# speedup vs baseline: 1.0337x; 1.0337x over previous
.Lkf_par_done:
	s_mov_b64 exec, -1
	v_lshlrev_b32_e32 v4, 4, v4
	v_lshlrev_b32_e32 v5, 6, v5
	v_lshl_or_b32 v3, v3, 2, v4
	v_lshlrev_b32_e32 v4, 4, v12
	v_or3_b32 v3, v3, v5, v2
	v_lshlrev_b32_e32 v5, 6, v13
	v_lshl_or_b32 v4, v11, 2, v4
	v_or3_b32 v43, v4, v5, v10
	v_lshlrev_b32_e32 v4, 4, v16
	v_lshlrev_b32_e32 v5, 6, v17
	v_lshl_or_b32 v4, v15, 2, v4
	v_lshlrev_b32_e32 v8, 4, v8
	v_or3_b32 v42, v4, v5, v14
	v_lshlrev_b32_e32 v4, 4, v20
	v_lshlrev_b32_e32 v9, 6, v9
	v_lshl_or_b32 v7, v7, 2, v8
	v_lshlrev_b32_e32 v5, 6, v21
	v_lshl_or_b32 v4, v19, 2, v4
	v_or3_b32 v44, v7, v9, v6
	v_or3_b32 v41, v4, v5, v18
	v_lshlrev_b32_e32 v4, 4, v24
	v_mov_b32_e32 v7, 0
	v_mov_b32_e32 v8, 0x64c
	v_lshlrev_b32_e32 v5, 6, v25
	v_lshl_or_b32 v4, v23, 2, v4
	s_waitcnt lgkmcnt(0)
	s_barrier
	ds_read_b96 v[36:38], v7 offset:1600
	ds_read_b64 v[16:17], v7 offset:1624
	ds_read2_b32 v[20:21], v8 offset1:1
	v_or3_b32 v19, v4, v5, v22
	v_lshlrev_b32_e32 v4, 4, v28
	v_lshlrev_b32_e32 v5, 6, v29
	v_lshl_or_b32 v4, v27, 2, v4
	v_or3_b32 v13, v4, v5, v26
	v_lshlrev_b32_e32 v4, 4, v32
	v_lshlrev_b32_e32 v5, 6, v33
	v_lshl_or_b32 v4, v31, 2, v4
	v_or3_b32 v9, v4, v5, v30
	s_waitcnt lgkmcnt(0)
	v_pk_fma_f32 v[4:5], v[76:77], v[20:21], v[16:17] op_sel_hi:[1,0,0]
	ds_read_b32 v8, v7 offset:1620
	ds_read_b32 v12, v7 offset:1632
	v_pk_fma_f32 v[4:5], v[78:79], v[36:37], v[4:5] op_sel_hi:[1,0,1]
	v_and_b32_e32 v6, 3, v6
	v_exp_f32_e32 v4, v4
	v_exp_f32_e32 v7, v5
	s_movk_i32 s3, 0xfff
	v_cmp_eq_u32_e32 vcc, 1, v6
	ds_read_b128 v[32:35], v134 offset:49152
	v_cvt_pknorm_u16_f32 v5, v4, v7
	v_lshrrev_b32_e32 v11, 4, v5
	v_bfe_u32 v15, v5, 4, 12
	v_bitop3_b32 v11, v11, s3, v11 bitop3:0xc
	v_mov_b32_e32 v15, v15
	v_mov_b32_e32 v11, 0x670
	v_lshl_add_u32 v25, v15, 2, v11
	v_mov_b32_e32 v15, 0x10000
	v_cndmask_b32_e32 v27, 1, v15, vcc
	v_bfe_u32 v23, v44, 2, 2
	ds_add_u32 v25, v27
	v_cndmask_b32_e32 v25, 0, v4, vcc
	v_lshrrev_b32_e32 v4, 20, v5
	v_xor_b32_e32 v5, 0xfff, v4
	v_cmp_eq_u32_e32 vcc, 1, v23
	v_mov_b32_e32 v24, v38
	s_nop 0
	v_mov_b32_e32 v4, v4
	v_lshl_add_u32 v27, v4, 2, v11
	v_pk_fma_f32 v[4:5], v[76:77], v[20:21], v[16:17] op_sel:[0,1,1]
	v_cndmask_b32_e32 v7, 0, v7, vcc
	v_pk_fma_f32 v[4:5], v[78:79], v[36:37], v[4:5] op_sel:[0,1,0]
	s_nop 0
	v_exp_f32_e32 v4, v4
	v_exp_f32_e32 v28, v5
	v_cndmask_b32_e32 v5, 1, v15, vcc
	ds_add_u32 v27, v5
	v_cmp_eq_u32_e32 vcc, 2, v6
	v_cvt_pknorm_u16_f32 v5, v4, v28
	v_lshrrev_b32_e32 v27, 4, v5
	v_bfe_u32 v29, v5, 4, 12
	v_bitop3_b32 v27, v27, s3, v27 bitop3:0xc
	v_cndmask_b32_e32 v25, v25, v4, vcc
	v_lshrrev_b32_e32 v4, 20, v5
	v_mov_b32_e32 v27, v29
	v_cndmask_b32_e32 v29, 1, v15, vcc
	v_xor_b32_e32 v5, 0xfff, v4
	v_cmp_eq_u32_e32 vcc, 2, v23
	v_lshl_add_u32 v27, v27, 2, v11
	ds_add_u32 v27, v29 offset:16384
	v_mov_b32_e32 v4, v4
	v_lshl_add_u32 v27, v4, 2, v11
	s_waitcnt lgkmcnt(4)
	v_pk_fma_f32 v[4:5], v[76:77], v[8:9], v[12:13] op_sel_hi:[1,0,0]
	v_cndmask_b32_e32 v29, 1, v15, vcc
	v_pk_fma_f32 v[4:5], v[78:79], v[24:25], v[4:5] op_sel_hi:[1,0,1]
	ds_add_u32 v27, v29 offset:16384
	v_exp_f32_e32 v4, v4
	v_exp_f32_e32 v5, v5
	v_cndmask_b32_e32 v7, v7, v28, vcc
	v_cmp_eq_u32_e32 vcc, 3, v6
	v_cvt_pknorm_u16_f32 v27, v4, v5
	v_lshrrev_b32_e32 v28, 4, v27
	v_bfe_u32 v29, v27, 4, 12
	v_bitop3_b32 v28, v28, s3, v28 bitop3:0xc
	v_mov_b32_e32 v6, v29
	v_lshl_add_u32 v6, v6, 2, v11
	v_cndmask_b32_e32 v28, 1, v15, vcc
	ds_add_u32 v6, v28 offset:32768
	v_lshrrev_b32_e32 v6, 20, v27
	v_cndmask_b32_e32 v4, v25, v4, vcc
	v_xor_b32_e32 v25, 0xfff, v6
	v_cmp_eq_u32_e32 vcc, 3, v23
	v_bfe_u32 v27, v44, 6, 2
	s_nop 0
	v_mov_b32_e32 v6, v6
	v_lshl_add_u32 v6, v6, 2, v11
	v_cndmask_b32_e32 v23, 1, v15, vcc
	ds_add_u32 v6, v23 offset:32768
	v_cndmask_b32_e32 v5, v7, v5, vcc
	v_pk_fma_f32 v[6:7], v[20:21], v[80:81], v[16:17] op_sel_hi:[0,1,0]
	v_pk_fma_f32 v[6:7], v[36:37], v[82:83], v[6:7] op_sel_hi:[0,1,1]
	v_exp_f32_e32 v6, v6
	v_exp_f32_e32 v23, v7
	v_bfe_u32 v25, v44, 4, 2
	v_cmp_eq_u32_e32 vcc, 1, v25
	s_waitcnt lgkmcnt(6)
	v_pk_add_f32 v[4:5], v[32:33], v[4:5] neg_lo:[0,1] neg_hi:[0,1]
	v_cvt_pknorm_u16_f32 v7, v6, v23
	v_lshrrev_b32_e32 v28, 4, v7
	v_bfe_u32 v29, v7, 4, 12
	v_bitop3_b32 v28, v28, s3, v28 bitop3:0xc
	v_mov_b32_e32 v28, v29
	v_lshl_add_u32 v28, v28, 2, v11
	v_cndmask_b32_e32 v29, 1, v15, vcc
	ds_add_u32 v28, v29
	v_cndmask_b32_e32 v28, 0, v6, vcc
	v_lshrrev_b32_e32 v6, 20, v7
	v_xor_b32_e32 v7, 0xfff, v6
	v_cmp_eq_u32_e32 vcc, 1, v27
	s_nop 1
	v_mov_b32_e32 v6, v6
	v_lshl_add_u32 v29, v6, 2, v11
	v_pk_fma_f32 v[6:7], v[20:21], v[80:81], v[16:17] op_sel:[1,0,1]
	v_cndmask_b32_e32 v23, 0, v23, vcc
	v_pk_fma_f32 v[6:7], v[36:37], v[82:83], v[6:7] op_sel:[1,0,0]
	s_nop 0
	v_exp_f32_e32 v6, v6
	v_exp_f32_e32 v31, v7
	v_cndmask_b32_e32 v7, 1, v15, vcc
	ds_add_u32 v29, v7
	v_cmp_eq_u32_e32 vcc, 2, v25
	v_cvt_pknorm_u16_f32 v7, v6, v31
	v_lshrrev_b32_e32 v29, 4, v7
	v_bfe_u32 v32, v7, 4, 12
	v_bitop3_b32 v29, v29, s3, v29 bitop3:0xc
	v_cndmask_b32_e32 v28, v28, v6, vcc
	v_lshrrev_b32_e32 v6, 20, v7
	v_mov_b32_e32 v29, v32
	v_cndmask_b32_e32 v32, 1, v15, vcc
	v_xor_b32_e32 v7, 0xfff, v6
	v_cmp_eq_u32_e32 vcc, 2, v27
	v_lshl_add_u32 v29, v29, 2, v11
	ds_add_u32 v29, v32 offset:16384
	v_mov_b32_e32 v6, v6
	v_lshl_add_u32 v29, v6, 2, v11
	v_pk_fma_f32 v[6:7], v[8:9], v[80:81], v[12:13] op_sel_hi:[0,1,0]
	v_pk_fma_f32 v[6:7], v[24:25], v[82:83], v[6:7] op_sel_hi:[0,1,1]
	v_exp_f32_e32 v6, v6
	v_exp_f32_e32 v7, v7
	v_cndmask_b32_e32 v32, 1, v15, vcc
	ds_add_u32 v29, v32 offset:16384
	v_cndmask_b32_e32 v23, v23, v31, vcc
	v_cvt_pknorm_u16_f32 v29, v6, v7
	v_lshrrev_b32_e32 v31, 4, v29
	v_bfe_u32 v32, v29, 4, 12
	v_bitop3_b32 v31, v31, s3, v31 bitop3:0xc
	v_cmp_eq_u32_e32 vcc, 3, v25
	s_nop 1
	v_mov_b32_e32 v25, v32
	v_lshl_add_u32 v25, v25, 2, v11
	v_cndmask_b32_e32 v31, 1, v15, vcc
	ds_add_u32 v25, v31 offset:32768
	v_lshrrev_b32_e32 v25, 20, v29
	v_cndmask_b32_e32 v6, v28, v6, vcc
	v_xor_b32_e32 v28, 0xfff, v25
	v_cmp_eq_u32_e32 vcc, 3, v27
	s_nop 1
	v_mov_b32_e32 v25, v25
	v_lshl_add_u32 v25, v25, 2, v11
	v_cndmask_b32_e32 v27, 1, v15, vcc
	ds_add_u32 v25, v27 offset:32768
	v_cndmask_b32_e32 v7, v23, v7, vcc
	v_pk_add_f32 v[6:7], v[34:35], v[6:7] neg_lo:[0,1] neg_hi:[0,1]
	s_nop 0
	v_pk_mul_f32 v[6:7], v[6:7], v[6:7]
	s_nop 0
	v_pk_fma_f32 v[28:29], v[4:5], v[4:5], v[6:7]
	ds_read_b128 v[76:79], v134 offset:61440
	v_mov_b32_e32 v164, 1
	v_mov_b32_e32 v165, 2
	v_mov_b32_e32 v150, 0
	v_mov_b32_e32 v151, 0
	v_mov_b32_e32 v152, 0
	v_mov_b32_e32 v153, 0
	v_and_b32_e32 v154, 3, v3
	v_bfe_u32 v155, v3, 2, 2
	v_bfe_u32 v156, v3, 4, 2
	v_bfe_u32 v157, v3, 6, 2
	s_mov_b32 s16, 0xfff0fff0
	v_pk_fma_f32 v[80:81], v[84:85], v[20:21], v[16:17] op_sel_hi:[1,0,0]
	v_pk_fma_f32 v[80:81], v[86:87], v[36:37], v[80:81] op_sel_hi:[1,0,1]
	s_nop 0
	v_exp_f32_e32 v82, v80
	v_exp_f32_e32 v83, v81
	v_cmp_eq_u32_e32 vcc, 1, v154
	v_cvt_pknorm_u16_f32 v158, v82, v83
	v_and_b32_e32 v159, s16, v158
	v_cndmask_b32_e32 v162, v164, v15, vcc
	v_cndmask_b32_e32 v150, v150, v82, vcc
	v_cmp_eq_u32_e32 vcc, 1, v155
	v_lshrrev_b32_sdwa v160, v165, v159 dst_sel:DWORD dst_unused:UNUSED_PAD src0_sel:DWORD src1_sel:WORD_0
	v_lshrrev_b32_sdwa v161, v165, v159 dst_sel:DWORD dst_unused:UNUSED_PAD src0_sel:DWORD src1_sel:WORD_1
	v_cndmask_b32_e32 v163, v164, v15, vcc
	v_cndmask_b32_e32 v151, v151, v83, vcc
	ds_add_u32 v160, v162 offset:1648
	ds_add_u32 v161, v163 offset:1648
	v_pk_fma_f32 v[80:81], v[84:85], v[20:21], v[16:17] op_sel:[0,1,1]
	v_pk_fma_f32 v[80:81], v[86:87], v[36:37], v[80:81] op_sel:[0,1,0]
	s_nop 0
	v_exp_f32_e32 v82, v80
	v_exp_f32_e32 v83, v81
	v_cmp_eq_u32_e32 vcc, 2, v154
	v_cvt_pknorm_u16_f32 v158, v82, v83
	v_and_b32_e32 v159, s16, v158
	v_cndmask_b32_e32 v162, v164, v15, vcc
	v_cndmask_b32_e32 v150, v150, v82, vcc
	v_cmp_eq_u32_e32 vcc, 2, v155
	v_lshrrev_b32_sdwa v160, v165, v159 dst_sel:DWORD dst_unused:UNUSED_PAD src0_sel:DWORD src1_sel:WORD_0
	v_lshrrev_b32_sdwa v161, v165, v159 dst_sel:DWORD dst_unused:UNUSED_PAD src0_sel:DWORD src1_sel:WORD_1
	v_cndmask_b32_e32 v163, v164, v15, vcc
	v_cndmask_b32_e32 v151, v151, v83, vcc
	ds_add_u32 v160, v162 offset:18032
	ds_add_u32 v161, v163 offset:18032
	v_pk_fma_f32 v[80:81], v[84:85], v[8:9], v[12:13] op_sel_hi:[1,0,0]
	v_pk_fma_f32 v[80:81], v[86:87], v[24:25], v[80:81] op_sel_hi:[1,0,1]
	s_nop 0
	v_exp_f32_e32 v82, v80
	v_exp_f32_e32 v83, v81
	v_cmp_eq_u32_e32 vcc, 3, v154
	v_cvt_pknorm_u16_f32 v158, v82, v83
	v_and_b32_e32 v159, s16, v158
	v_cndmask_b32_e32 v162, v164, v15, vcc
	v_cndmask_b32_e32 v150, v150, v82, vcc
	v_cmp_eq_u32_e32 vcc, 3, v155
	v_lshrrev_b32_sdwa v160, v165, v159 dst_sel:DWORD dst_unused:UNUSED_PAD src0_sel:DWORD src1_sel:WORD_0
	v_lshrrev_b32_sdwa v161, v165, v159 dst_sel:DWORD dst_unused:UNUSED_PAD src0_sel:DWORD src1_sel:WORD_1
	v_cndmask_b32_e32 v163, v164, v15, vcc
	v_cndmask_b32_e32 v151, v151, v83, vcc
	ds_add_u32 v160, v162 offset:34416
	ds_add_u32 v161, v163 offset:34416
	s_waitcnt lgkmcnt(6)
	v_pk_add_f32 v[166:167], v[76:77], v[150:151] neg_lo:[0,1] neg_hi:[0,1]
	s_nop 0
	v_pk_fma_f32 v[166:167], v[166:167], v[166:167], v[28:29]
	v_pk_fma_f32 v[80:81], v[88:89], v[20:21], v[16:17] op_sel_hi:[1,0,0]
	v_pk_fma_f32 v[80:81], v[90:91], v[36:37], v[80:81] op_sel_hi:[1,0,1]
	s_nop 0
	v_exp_f32_e32 v82, v80
	v_exp_f32_e32 v83, v81
	v_cmp_eq_u32_e32 vcc, 1, v156
	v_cvt_pknorm_u16_f32 v158, v82, v83
	v_and_b32_e32 v159, s16, v158
	v_cndmask_b32_e32 v162, v164, v15, vcc
	v_cndmask_b32_e32 v152, v152, v82, vcc
	v_cmp_eq_u32_e32 vcc, 1, v157
	v_lshrrev_b32_sdwa v160, v165, v159 dst_sel:DWORD dst_unused:UNUSED_PAD src0_sel:DWORD src1_sel:WORD_0
	v_lshrrev_b32_sdwa v161, v165, v159 dst_sel:DWORD dst_unused:UNUSED_PAD src0_sel:DWORD src1_sel:WORD_1
	v_cndmask_b32_e32 v163, v164, v15, vcc
	v_cndmask_b32_e32 v153, v153, v83, vcc
	ds_add_u32 v160, v162 offset:1648
	ds_add_u32 v161, v163 offset:1648
	v_pk_fma_f32 v[80:81], v[88:89], v[20:21], v[16:17] op_sel:[0,1,1]
	v_pk_fma_f32 v[80:81], v[90:91], v[36:37], v[80:81] op_sel:[0,1,0]
	s_nop 0
	v_exp_f32_e32 v82, v80
	v_exp_f32_e32 v83, v81
	v_cmp_eq_u32_e32 vcc, 2, v156
	v_cvt_pknorm_u16_f32 v158, v82, v83
	v_and_b32_e32 v159, s16, v158
	v_cndmask_b32_e32 v162, v164, v15, vcc
	v_cndmask_b32_e32 v152, v152, v82, vcc
	v_cmp_eq_u32_e32 vcc, 2, v157
	v_lshrrev_b32_sdwa v160, v165, v159 dst_sel:DWORD dst_unused:UNUSED_PAD src0_sel:DWORD src1_sel:WORD_0
	v_lshrrev_b32_sdwa v161, v165, v159 dst_sel:DWORD dst_unused:UNUSED_PAD src0_sel:DWORD src1_sel:WORD_1
	v_cndmask_b32_e32 v163, v164, v15, vcc
	v_cndmask_b32_e32 v153, v153, v83, vcc
	ds_add_u32 v160, v162 offset:18032
	ds_add_u32 v161, v163 offset:18032
	v_pk_fma_f32 v[80:81], v[88:89], v[8:9], v[12:13] op_sel_hi:[1,0,0]
	v_pk_fma_f32 v[80:81], v[90:91], v[24:25], v[80:81] op_sel_hi:[1,0,1]
	s_nop 0
	v_exp_f32_e32 v82, v80
	v_exp_f32_e32 v83, v81
	v_cmp_eq_u32_e32 vcc, 3, v156
	v_cvt_pknorm_u16_f32 v158, v82, v83
	v_and_b32_e32 v159, s16, v158
	v_cndmask_b32_e32 v162, v164, v15, vcc
	v_cndmask_b32_e32 v152, v152, v82, vcc
	v_cmp_eq_u32_e32 vcc, 3, v157
	v_lshrrev_b32_sdwa v160, v165, v159 dst_sel:DWORD dst_unused:UNUSED_PAD src0_sel:DWORD src1_sel:WORD_0
	v_lshrrev_b32_sdwa v161, v165, v159 dst_sel:DWORD dst_unused:UNUSED_PAD src0_sel:DWORD src1_sel:WORD_1
	v_cndmask_b32_e32 v163, v164, v15, vcc
	v_cndmask_b32_e32 v153, v153, v83, vcc
	ds_add_u32 v160, v162 offset:34416
	ds_add_u32 v161, v163 offset:34416
	v_pk_add_f32 v[80:81], v[78:79], v[152:153] neg_lo:[0,1] neg_hi:[0,1]
	s_nop 0
	v_pk_fma_f32 v[6:7], v[80:81], v[80:81], v[166:167]
	ds_read_b128 v[76:79], v1 offset:24576
	v_mov_b32_e32 v164, 1
	v_mov_b32_e32 v165, 2
	v_mov_b32_e32 v150, 0
	v_mov_b32_e32 v151, 0
	v_mov_b32_e32 v152, 0
	v_mov_b32_e32 v153, 0
	v_and_b32_e32 v154, 3, v43
	v_bfe_u32 v155, v43, 2, 2
	v_bfe_u32 v156, v43, 4, 2
	v_bfe_u32 v157, v43, 6, 2
	s_mov_b32 s16, 0xfff0fff0
	v_pk_fma_f32 v[80:81], v[92:93], v[20:21], v[16:17] op_sel_hi:[1,0,0]
	v_pk_fma_f32 v[80:81], v[94:95], v[36:37], v[80:81] op_sel_hi:[1,0,1]
	s_nop 0
	v_exp_f32_e32 v82, v80
	v_exp_f32_e32 v83, v81
	v_cmp_eq_u32_e32 vcc, 1, v154
	v_cvt_pknorm_u16_f32 v158, v82, v83
	v_and_b32_e32 v159, s16, v158
	v_cndmask_b32_e32 v162, v164, v15, vcc
	v_cndmask_b32_e32 v150, v150, v82, vcc
	v_cmp_eq_u32_e32 vcc, 1, v155
	v_lshrrev_b32_sdwa v160, v165, v159 dst_sel:DWORD dst_unused:UNUSED_PAD src0_sel:DWORD src1_sel:WORD_0
	v_lshrrev_b32_sdwa v161, v165, v159 dst_sel:DWORD dst_unused:UNUSED_PAD src0_sel:DWORD src1_sel:WORD_1
	v_cndmask_b32_e32 v163, v164, v15, vcc
	v_cndmask_b32_e32 v151, v151, v83, vcc
	ds_add_u32 v160, v162 offset:1648
	ds_add_u32 v161, v163 offset:1648
	v_pk_fma_f32 v[80:81], v[92:93], v[20:21], v[16:17] op_sel:[0,1,1]
	v_pk_fma_f32 v[80:81], v[94:95], v[36:37], v[80:81] op_sel:[0,1,0]
	s_nop 0
	v_exp_f32_e32 v82, v80
	v_exp_f32_e32 v83, v81
	v_cmp_eq_u32_e32 vcc, 2, v154
	v_cvt_pknorm_u16_f32 v158, v82, v83
	v_and_b32_e32 v159, s16, v158
	v_cndmask_b32_e32 v162, v164, v15, vcc
	v_cndmask_b32_e32 v150, v150, v82, vcc
	v_cmp_eq_u32_e32 vcc, 2, v155
	v_lshrrev_b32_sdwa v160, v165, v159 dst_sel:DWORD dst_unused:UNUSED_PAD src0_sel:DWORD src1_sel:WORD_0
	v_lshrrev_b32_sdwa v161, v165, v159 dst_sel:DWORD dst_unused:UNUSED_PAD src0_sel:DWORD src1_sel:WORD_1
	v_cndmask_b32_e32 v163, v164, v15, vcc
	v_cndmask_b32_e32 v151, v151, v83, vcc
	ds_add_u32 v160, v162 offset:18032
	ds_add_u32 v161, v163 offset:18032
	v_pk_fma_f32 v[80:81], v[92:93], v[8:9], v[12:13] op_sel_hi:[1,0,0]
	v_pk_fma_f32 v[80:81], v[94:95], v[24:25], v[80:81] op_sel_hi:[1,0,1]
	s_nop 0
	v_exp_f32_e32 v82, v80
	v_exp_f32_e32 v83, v81
	v_cmp_eq_u32_e32 vcc, 3, v154
	v_cvt_pknorm_u16_f32 v158, v82, v83
	v_and_b32_e32 v159, s16, v158
	v_cndmask_b32_e32 v162, v164, v15, vcc
	v_cndmask_b32_e32 v150, v150, v82, vcc
	v_cmp_eq_u32_e32 vcc, 3, v155
	v_lshrrev_b32_sdwa v160, v165, v159 dst_sel:DWORD dst_unused:UNUSED_PAD src0_sel:DWORD src1_sel:WORD_0
	v_lshrrev_b32_sdwa v161, v165, v159 dst_sel:DWORD dst_unused:UNUSED_PAD src0_sel:DWORD src1_sel:WORD_1
	v_cndmask_b32_e32 v163, v164, v15, vcc
	v_cndmask_b32_e32 v151, v151, v83, vcc
	ds_add_u32 v160, v162 offset:34416
	ds_add_u32 v161, v163 offset:34416
	s_waitcnt lgkmcnt(6)
	v_pk_add_f32 v[166:167], v[76:77], v[150:151] neg_lo:[0,1] neg_hi:[0,1]
	s_nop 0
	v_pk_fma_f32 v[166:167], v[166:167], v[166:167], v[6:7]
	v_pk_fma_f32 v[80:81], v[96:97], v[20:21], v[16:17] op_sel_hi:[1,0,0]
	v_pk_fma_f32 v[80:81], v[98:99], v[36:37], v[80:81] op_sel_hi:[1,0,1]
	s_nop 0
	v_exp_f32_e32 v82, v80
	v_exp_f32_e32 v83, v81
	v_cmp_eq_u32_e32 vcc, 1, v156
	v_cvt_pknorm_u16_f32 v158, v82, v83
	v_and_b32_e32 v159, s16, v158
	v_cndmask_b32_e32 v162, v164, v15, vcc
	v_cndmask_b32_e32 v152, v152, v82, vcc
	v_cmp_eq_u32_e32 vcc, 1, v157
	v_lshrrev_b32_sdwa v160, v165, v159 dst_sel:DWORD dst_unused:UNUSED_PAD src0_sel:DWORD src1_sel:WORD_0
	v_lshrrev_b32_sdwa v161, v165, v159 dst_sel:DWORD dst_unused:UNUSED_PAD src0_sel:DWORD src1_sel:WORD_1
	v_cndmask_b32_e32 v163, v164, v15, vcc
	v_cndmask_b32_e32 v153, v153, v83, vcc
	ds_add_u32 v160, v162 offset:1648
	ds_add_u32 v161, v163 offset:1648
	v_pk_fma_f32 v[80:81], v[96:97], v[20:21], v[16:17] op_sel:[0,1,1]
	v_pk_fma_f32 v[80:81], v[98:99], v[36:37], v[80:81] op_sel:[0,1,0]
	s_nop 0
	v_exp_f32_e32 v82, v80
	v_exp_f32_e32 v83, v81
	v_cmp_eq_u32_e32 vcc, 2, v156
	v_cvt_pknorm_u16_f32 v158, v82, v83
	v_and_b32_e32 v159, s16, v158
	v_cndmask_b32_e32 v162, v164, v15, vcc
	v_cndmask_b32_e32 v152, v152, v82, vcc
	v_cmp_eq_u32_e32 vcc, 2, v157
	v_lshrrev_b32_sdwa v160, v165, v159 dst_sel:DWORD dst_unused:UNUSED_PAD src0_sel:DWORD src1_sel:WORD_0
	v_lshrrev_b32_sdwa v161, v165, v159 dst_sel:DWORD dst_unused:UNUSED_PAD src0_sel:DWORD src1_sel:WORD_1
	v_cndmask_b32_e32 v163, v164, v15, vcc
	v_cndmask_b32_e32 v153, v153, v83, vcc
	ds_add_u32 v160, v162 offset:18032
	ds_add_u32 v161, v163 offset:18032
	v_pk_fma_f32 v[80:81], v[96:97], v[8:9], v[12:13] op_sel_hi:[1,0,0]
	v_pk_fma_f32 v[80:81], v[98:99], v[24:25], v[80:81] op_sel_hi:[1,0,1]
	s_nop 0
	v_exp_f32_e32 v82, v80
	v_exp_f32_e32 v83, v81
	v_cmp_eq_u32_e32 vcc, 3, v156
	v_cvt_pknorm_u16_f32 v158, v82, v83
	v_and_b32_e32 v159, s16, v158
	v_cndmask_b32_e32 v162, v164, v15, vcc
	v_cndmask_b32_e32 v152, v152, v82, vcc
	v_cmp_eq_u32_e32 vcc, 3, v157
	v_lshrrev_b32_sdwa v160, v165, v159 dst_sel:DWORD dst_unused:UNUSED_PAD src0_sel:DWORD src1_sel:WORD_0
	v_lshrrev_b32_sdwa v161, v165, v159 dst_sel:DWORD dst_unused:UNUSED_PAD src0_sel:DWORD src1_sel:WORD_1
	v_cndmask_b32_e32 v163, v164, v15, vcc
	v_cndmask_b32_e32 v153, v153, v83, vcc
	ds_add_u32 v160, v162 offset:34416
	ds_add_u32 v161, v163 offset:34416
	v_pk_add_f32 v[80:81], v[78:79], v[152:153] neg_lo:[0,1] neg_hi:[0,1]
	s_nop 0
	v_pk_fma_f32 v[6:7], v[80:81], v[80:81], v[166:167]
	ds_read_b128 v[76:79], v1 offset:36864
	v_mov_b32_e32 v164, 1
	v_mov_b32_e32 v165, 2
	v_mov_b32_e32 v150, 0
	v_mov_b32_e32 v151, 0
	v_mov_b32_e32 v152, 0
	v_mov_b32_e32 v153, 0
	v_and_b32_e32 v154, 3, v42
	v_bfe_u32 v155, v42, 2, 2
	v_bfe_u32 v156, v42, 4, 2
	v_bfe_u32 v157, v42, 6, 2
	s_mov_b32 s16, 0xfff0fff0
	v_pk_fma_f32 v[80:81], v[100:101], v[20:21], v[16:17] op_sel_hi:[1,0,0]
	v_pk_fma_f32 v[80:81], v[102:103], v[36:37], v[80:81] op_sel_hi:[1,0,1]
	s_nop 0
	v_exp_f32_e32 v82, v80
	v_exp_f32_e32 v83, v81
	v_cmp_eq_u32_e32 vcc, 1, v154
	v_cvt_pknorm_u16_f32 v158, v82, v83
	v_and_b32_e32 v159, s16, v158
	v_cndmask_b32_e32 v162, v164, v15, vcc
	v_cndmask_b32_e32 v150, v150, v82, vcc
	v_cmp_eq_u32_e32 vcc, 1, v155
	v_lshrrev_b32_sdwa v160, v165, v159 dst_sel:DWORD dst_unused:UNUSED_PAD src0_sel:DWORD src1_sel:WORD_0
	v_lshrrev_b32_sdwa v161, v165, v159 dst_sel:DWORD dst_unused:UNUSED_PAD src0_sel:DWORD src1_sel:WORD_1
	v_cndmask_b32_e32 v163, v164, v15, vcc
	v_cndmask_b32_e32 v151, v151, v83, vcc
	ds_add_u32 v160, v162 offset:1648
	ds_add_u32 v161, v163 offset:1648
	v_pk_fma_f32 v[80:81], v[100:101], v[20:21], v[16:17] op_sel:[0,1,1]
	v_pk_fma_f32 v[80:81], v[102:103], v[36:37], v[80:81] op_sel:[0,1,0]
	s_nop 0
	v_exp_f32_e32 v82, v80
	v_exp_f32_e32 v83, v81
	v_cmp_eq_u32_e32 vcc, 2, v154
	v_cvt_pknorm_u16_f32 v158, v82, v83
	v_and_b32_e32 v159, s16, v158
	v_cndmask_b32_e32 v162, v164, v15, vcc
	v_cndmask_b32_e32 v150, v150, v82, vcc
	v_cmp_eq_u32_e32 vcc, 2, v155
	v_lshrrev_b32_sdwa v160, v165, v159 dst_sel:DWORD dst_unused:UNUSED_PAD src0_sel:DWORD src1_sel:WORD_0
	v_lshrrev_b32_sdwa v161, v165, v159 dst_sel:DWORD dst_unused:UNUSED_PAD src0_sel:DWORD src1_sel:WORD_1
	v_cndmask_b32_e32 v163, v164, v15, vcc
	v_cndmask_b32_e32 v151, v151, v83, vcc
	ds_add_u32 v160, v162 offset:18032
	ds_add_u32 v161, v163 offset:18032
	v_pk_fma_f32 v[80:81], v[100:101], v[8:9], v[12:13] op_sel_hi:[1,0,0]
	v_pk_fma_f32 v[80:81], v[102:103], v[24:25], v[80:81] op_sel_hi:[1,0,1]
	s_nop 0
	v_exp_f32_e32 v82, v80
	v_exp_f32_e32 v83, v81
	v_cmp_eq_u32_e32 vcc, 3, v154
	v_cvt_pknorm_u16_f32 v158, v82, v83
	v_and_b32_e32 v159, s16, v158
	v_cndmask_b32_e32 v162, v164, v15, vcc
	v_cndmask_b32_e32 v150, v150, v82, vcc
	v_cmp_eq_u32_e32 vcc, 3, v155
	v_lshrrev_b32_sdwa v160, v165, v159 dst_sel:DWORD dst_unused:UNUSED_PAD src0_sel:DWORD src1_sel:WORD_0
	v_lshrrev_b32_sdwa v161, v165, v159 dst_sel:DWORD dst_unused:UNUSED_PAD src0_sel:DWORD src1_sel:WORD_1
	v_cndmask_b32_e32 v163, v164, v15, vcc
	v_cndmask_b32_e32 v151, v151, v83, vcc
	ds_add_u32 v160, v162 offset:34416
	ds_add_u32 v161, v163 offset:34416
	s_waitcnt lgkmcnt(6)
	v_pk_add_f32 v[166:167], v[76:77], v[150:151] neg_lo:[0,1] neg_hi:[0,1]
	s_nop 0
	v_pk_fma_f32 v[166:167], v[166:167], v[166:167], v[6:7]
	v_pk_fma_f32 v[80:81], v[104:105], v[20:21], v[16:17] op_sel_hi:[1,0,0]
	v_pk_fma_f32 v[80:81], v[106:107], v[36:37], v[80:81] op_sel_hi:[1,0,1]
	s_nop 0
	v_exp_f32_e32 v82, v80
	v_exp_f32_e32 v83, v81
	v_cmp_eq_u32_e32 vcc, 1, v156
	v_cvt_pknorm_u16_f32 v158, v82, v83
	v_and_b32_e32 v159, s16, v158
	v_cndmask_b32_e32 v162, v164, v15, vcc
	v_cndmask_b32_e32 v152, v152, v82, vcc
	v_cmp_eq_u32_e32 vcc, 1, v157
	v_lshrrev_b32_sdwa v160, v165, v159 dst_sel:DWORD dst_unused:UNUSED_PAD src0_sel:DWORD src1_sel:WORD_0
	v_lshrrev_b32_sdwa v161, v165, v159 dst_sel:DWORD dst_unused:UNUSED_PAD src0_sel:DWORD src1_sel:WORD_1
	v_cndmask_b32_e32 v163, v164, v15, vcc
	v_cndmask_b32_e32 v153, v153, v83, vcc
	ds_add_u32 v160, v162 offset:1648
	ds_add_u32 v161, v163 offset:1648
	v_pk_fma_f32 v[80:81], v[104:105], v[20:21], v[16:17] op_sel:[0,1,1]
	v_pk_fma_f32 v[80:81], v[106:107], v[36:37], v[80:81] op_sel:[0,1,0]
	s_nop 0
	v_exp_f32_e32 v82, v80
	v_exp_f32_e32 v83, v81
	v_cmp_eq_u32_e32 vcc, 2, v156
	v_cvt_pknorm_u16_f32 v158, v82, v83
	v_and_b32_e32 v159, s16, v158
	v_cndmask_b32_e32 v162, v164, v15, vcc
	v_cndmask_b32_e32 v152, v152, v82, vcc
	v_cmp_eq_u32_e32 vcc, 2, v157
	v_lshrrev_b32_sdwa v160, v165, v159 dst_sel:DWORD dst_unused:UNUSED_PAD src0_sel:DWORD src1_sel:WORD_0
	v_lshrrev_b32_sdwa v161, v165, v159 dst_sel:DWORD dst_unused:UNUSED_PAD src0_sel:DWORD src1_sel:WORD_1
	v_cndmask_b32_e32 v163, v164, v15, vcc
	v_cndmask_b32_e32 v153, v153, v83, vcc
	ds_add_u32 v160, v162 offset:18032
	ds_add_u32 v161, v163 offset:18032
	v_pk_fma_f32 v[80:81], v[104:105], v[8:9], v[12:13] op_sel_hi:[1,0,0]
	v_pk_fma_f32 v[80:81], v[106:107], v[24:25], v[80:81] op_sel_hi:[1,0,1]
	s_nop 0
	v_exp_f32_e32 v82, v80
	v_exp_f32_e32 v83, v81
	v_cmp_eq_u32_e32 vcc, 3, v156
	v_cvt_pknorm_u16_f32 v158, v82, v83
	v_and_b32_e32 v159, s16, v158
	v_cndmask_b32_e32 v162, v164, v15, vcc
	v_cndmask_b32_e32 v152, v152, v82, vcc
	v_cmp_eq_u32_e32 vcc, 3, v157
	v_lshrrev_b32_sdwa v160, v165, v159 dst_sel:DWORD dst_unused:UNUSED_PAD src0_sel:DWORD src1_sel:WORD_0
	v_lshrrev_b32_sdwa v161, v165, v159 dst_sel:DWORD dst_unused:UNUSED_PAD src0_sel:DWORD src1_sel:WORD_1
	v_cndmask_b32_e32 v163, v164, v15, vcc
	v_cndmask_b32_e32 v153, v153, v83, vcc
	ds_add_u32 v160, v162 offset:34416
	ds_add_u32 v161, v163 offset:34416
	v_pk_add_f32 v[80:81], v[78:79], v[152:153] neg_lo:[0,1] neg_hi:[0,1]
	s_nop 0
	v_pk_fma_f32 v[6:7], v[80:81], v[80:81], v[166:167]
	ds_read_b128 v[76:79], v1 offset:49152
	v_mov_b32_e32 v164, 1
	v_mov_b32_e32 v165, 2
	v_mov_b32_e32 v150, 0
	v_mov_b32_e32 v151, 0
	v_mov_b32_e32 v152, 0
	v_mov_b32_e32 v153, 0
	v_and_b32_e32 v154, 3, v41
	v_bfe_u32 v155, v41, 2, 2
	v_bfe_u32 v156, v41, 4, 2
	v_bfe_u32 v157, v41, 6, 2
	s_mov_b32 s16, 0xfff0fff0
	v_pk_fma_f32 v[80:81], v[108:109], v[20:21], v[16:17] op_sel_hi:[1,0,0]
	v_pk_fma_f32 v[80:81], v[110:111], v[36:37], v[80:81] op_sel_hi:[1,0,1]
	s_nop 0
	v_exp_f32_e32 v82, v80
	v_exp_f32_e32 v83, v81
	v_cmp_eq_u32_e32 vcc, 1, v154
	v_cvt_pknorm_u16_f32 v158, v82, v83
	v_and_b32_e32 v159, s16, v158
	v_cndmask_b32_e32 v162, v164, v15, vcc
	v_cndmask_b32_e32 v150, v150, v82, vcc
	v_cmp_eq_u32_e32 vcc, 1, v155
	v_lshrrev_b32_sdwa v160, v165, v159 dst_sel:DWORD dst_unused:UNUSED_PAD src0_sel:DWORD src1_sel:WORD_0
	v_lshrrev_b32_sdwa v161, v165, v159 dst_sel:DWORD dst_unused:UNUSED_PAD src0_sel:DWORD src1_sel:WORD_1
	v_cndmask_b32_e32 v163, v164, v15, vcc
	v_cndmask_b32_e32 v151, v151, v83, vcc
	ds_add_u32 v160, v162 offset:1648
	ds_add_u32 v161, v163 offset:1648
	v_pk_fma_f32 v[80:81], v[108:109], v[20:21], v[16:17] op_sel:[0,1,1]
	v_pk_fma_f32 v[80:81], v[110:111], v[36:37], v[80:81] op_sel:[0,1,0]
	s_nop 0
	v_exp_f32_e32 v82, v80
	v_exp_f32_e32 v83, v81
	v_cmp_eq_u32_e32 vcc, 2, v154
	v_cvt_pknorm_u16_f32 v158, v82, v83
	v_and_b32_e32 v159, s16, v158
	v_cndmask_b32_e32 v162, v164, v15, vcc
	v_cndmask_b32_e32 v150, v150, v82, vcc
	v_cmp_eq_u32_e32 vcc, 2, v155
	v_lshrrev_b32_sdwa v160, v165, v159 dst_sel:DWORD dst_unused:UNUSED_PAD src0_sel:DWORD src1_sel:WORD_0
	v_lshrrev_b32_sdwa v161, v165, v159 dst_sel:DWORD dst_unused:UNUSED_PAD src0_sel:DWORD src1_sel:WORD_1
	v_cndmask_b32_e32 v163, v164, v15, vcc
	v_cndmask_b32_e32 v151, v151, v83, vcc
	ds_add_u32 v160, v162 offset:18032
	ds_add_u32 v161, v163 offset:18032
	v_pk_fma_f32 v[80:81], v[108:109], v[8:9], v[12:13] op_sel_hi:[1,0,0]
	v_pk_fma_f32 v[80:81], v[110:111], v[24:25], v[80:81] op_sel_hi:[1,0,1]
	s_nop 0
	v_exp_f32_e32 v82, v80
	v_exp_f32_e32 v83, v81
	v_cmp_eq_u32_e32 vcc, 3, v154
	v_cvt_pknorm_u16_f32 v158, v82, v83
	v_and_b32_e32 v159, s16, v158
	v_cndmask_b32_e32 v162, v164, v15, vcc
	v_cndmask_b32_e32 v150, v150, v82, vcc
	v_cmp_eq_u32_e32 vcc, 3, v155
	v_lshrrev_b32_sdwa v160, v165, v159 dst_sel:DWORD dst_unused:UNUSED_PAD src0_sel:DWORD src1_sel:WORD_0
	v_lshrrev_b32_sdwa v161, v165, v159 dst_sel:DWORD dst_unused:UNUSED_PAD src0_sel:DWORD src1_sel:WORD_1
	v_cndmask_b32_e32 v163, v164, v15, vcc
	v_cndmask_b32_e32 v151, v151, v83, vcc
	ds_add_u32 v160, v162 offset:34416
	ds_add_u32 v161, v163 offset:34416
	s_waitcnt lgkmcnt(6)
	v_pk_add_f32 v[166:167], v[76:77], v[150:151] neg_lo:[0,1] neg_hi:[0,1]
	s_nop 0
	v_pk_fma_f32 v[166:167], v[166:167], v[166:167], v[6:7]
	v_pk_fma_f32 v[80:81], v[112:113], v[20:21], v[16:17] op_sel_hi:[1,0,0]
	v_pk_fma_f32 v[80:81], v[114:115], v[36:37], v[80:81] op_sel_hi:[1,0,1]
	s_nop 0
	v_exp_f32_e32 v82, v80
	v_exp_f32_e32 v83, v81
	v_cmp_eq_u32_e32 vcc, 1, v156
	v_cvt_pknorm_u16_f32 v158, v82, v83
	v_and_b32_e32 v159, s16, v158
	v_cndmask_b32_e32 v162, v164, v15, vcc
	v_cndmask_b32_e32 v152, v152, v82, vcc
	v_cmp_eq_u32_e32 vcc, 1, v157
	v_lshrrev_b32_sdwa v160, v165, v159 dst_sel:DWORD dst_unused:UNUSED_PAD src0_sel:DWORD src1_sel:WORD_0
	v_lshrrev_b32_sdwa v161, v165, v159 dst_sel:DWORD dst_unused:UNUSED_PAD src0_sel:DWORD src1_sel:WORD_1
	v_cndmask_b32_e32 v163, v164, v15, vcc
	v_cndmask_b32_e32 v153, v153, v83, vcc
	ds_add_u32 v160, v162 offset:1648
	ds_add_u32 v161, v163 offset:1648
	v_pk_fma_f32 v[80:81], v[112:113], v[20:21], v[16:17] op_sel:[0,1,1]
	v_pk_fma_f32 v[80:81], v[114:115], v[36:37], v[80:81] op_sel:[0,1,0]
	s_nop 0
	v_exp_f32_e32 v82, v80
	v_exp_f32_e32 v83, v81
	v_cmp_eq_u32_e32 vcc, 2, v156
	v_cvt_pknorm_u16_f32 v158, v82, v83
	v_and_b32_e32 v159, s16, v158
	v_cndmask_b32_e32 v162, v164, v15, vcc
	v_cndmask_b32_e32 v152, v152, v82, vcc
	v_cmp_eq_u32_e32 vcc, 2, v157
	v_lshrrev_b32_sdwa v160, v165, v159 dst_sel:DWORD dst_unused:UNUSED_PAD src0_sel:DWORD src1_sel:WORD_0
	v_lshrrev_b32_sdwa v161, v165, v159 dst_sel:DWORD dst_unused:UNUSED_PAD src0_sel:DWORD src1_sel:WORD_1
	v_cndmask_b32_e32 v163, v164, v15, vcc
	v_cndmask_b32_e32 v153, v153, v83, vcc
	ds_add_u32 v160, v162 offset:18032
	ds_add_u32 v161, v163 offset:18032
	v_pk_fma_f32 v[80:81], v[112:113], v[8:9], v[12:13] op_sel_hi:[1,0,0]
	v_pk_fma_f32 v[80:81], v[114:115], v[24:25], v[80:81] op_sel_hi:[1,0,1]
	s_nop 0
	v_exp_f32_e32 v82, v80
	v_exp_f32_e32 v83, v81
	v_cmp_eq_u32_e32 vcc, 3, v156
	v_cvt_pknorm_u16_f32 v158, v82, v83
	v_and_b32_e32 v159, s16, v158
	v_cndmask_b32_e32 v162, v164, v15, vcc
	v_cndmask_b32_e32 v152, v152, v82, vcc
	v_cmp_eq_u32_e32 vcc, 3, v157
	v_lshrrev_b32_sdwa v160, v165, v159 dst_sel:DWORD dst_unused:UNUSED_PAD src0_sel:DWORD src1_sel:WORD_0
	v_lshrrev_b32_sdwa v161, v165, v159 dst_sel:DWORD dst_unused:UNUSED_PAD src0_sel:DWORD src1_sel:WORD_1
	v_cndmask_b32_e32 v163, v164, v15, vcc
	v_cndmask_b32_e32 v153, v153, v83, vcc
	ds_add_u32 v160, v162 offset:34416
	ds_add_u32 v161, v163 offset:34416
	v_pk_add_f32 v[80:81], v[78:79], v[152:153] neg_lo:[0,1] neg_hi:[0,1]
	s_nop 0
	v_pk_fma_f32 v[6:7], v[80:81], v[80:81], v[166:167]
	ds_read_b128 v[76:79], v1 offset:61440
	v_mov_b32_e32 v164, 1
	v_mov_b32_e32 v165, 2
	v_mov_b32_e32 v150, 0
	v_mov_b32_e32 v151, 0
	v_mov_b32_e32 v152, 0
	v_mov_b32_e32 v153, 0
	v_and_b32_e32 v154, 3, v19
	v_bfe_u32 v155, v19, 2, 2
	v_bfe_u32 v156, v19, 4, 2
	v_bfe_u32 v157, v19, 6, 2
	s_mov_b32 s16, 0xfff0fff0
	v_pk_fma_f32 v[80:81], v[116:117], v[20:21], v[16:17] op_sel_hi:[1,0,0]
	v_pk_fma_f32 v[80:81], v[118:119], v[36:37], v[80:81] op_sel_hi:[1,0,1]
	s_nop 0
	v_exp_f32_e32 v82, v80
	v_exp_f32_e32 v83, v81
	v_cmp_eq_u32_e32 vcc, 1, v154
	v_cvt_pknorm_u16_f32 v158, v82, v83
	v_and_b32_e32 v159, s16, v158
	v_cndmask_b32_e32 v162, v164, v15, vcc
	v_cndmask_b32_e32 v150, v150, v82, vcc
	v_cmp_eq_u32_e32 vcc, 1, v155
	v_lshrrev_b32_sdwa v160, v165, v159 dst_sel:DWORD dst_unused:UNUSED_PAD src0_sel:DWORD src1_sel:WORD_0
	v_lshrrev_b32_sdwa v161, v165, v159 dst_sel:DWORD dst_unused:UNUSED_PAD src0_sel:DWORD src1_sel:WORD_1
	v_cndmask_b32_e32 v163, v164, v15, vcc
	v_cndmask_b32_e32 v151, v151, v83, vcc
	ds_add_u32 v160, v162 offset:1648
	ds_add_u32 v161, v163 offset:1648
	v_pk_fma_f32 v[80:81], v[116:117], v[20:21], v[16:17] op_sel:[0,1,1]
	v_pk_fma_f32 v[80:81], v[118:119], v[36:37], v[80:81] op_sel:[0,1,0]
	s_nop 0
	v_exp_f32_e32 v82, v80
	v_exp_f32_e32 v83, v81
	v_cmp_eq_u32_e32 vcc, 2, v154
	v_cvt_pknorm_u16_f32 v158, v82, v83
	v_and_b32_e32 v159, s16, v158
	v_cndmask_b32_e32 v162, v164, v15, vcc
	v_cndmask_b32_e32 v150, v150, v82, vcc
	v_cmp_eq_u32_e32 vcc, 2, v155
	v_lshrrev_b32_sdwa v160, v165, v159 dst_sel:DWORD dst_unused:UNUSED_PAD src0_sel:DWORD src1_sel:WORD_0
	v_lshrrev_b32_sdwa v161, v165, v159 dst_sel:DWORD dst_unused:UNUSED_PAD src0_sel:DWORD src1_sel:WORD_1
	v_cndmask_b32_e32 v163, v164, v15, vcc
	v_cndmask_b32_e32 v151, v151, v83, vcc
	ds_add_u32 v160, v162 offset:18032
	ds_add_u32 v161, v163 offset:18032
	v_pk_fma_f32 v[80:81], v[116:117], v[8:9], v[12:13] op_sel_hi:[1,0,0]
	v_pk_fma_f32 v[80:81], v[118:119], v[24:25], v[80:81] op_sel_hi:[1,0,1]
	s_nop 0
	v_exp_f32_e32 v82, v80
	v_exp_f32_e32 v83, v81
	v_cmp_eq_u32_e32 vcc, 3, v154
	v_cvt_pknorm_u16_f32 v158, v82, v83
	v_and_b32_e32 v159, s16, v158
	v_cndmask_b32_e32 v162, v164, v15, vcc
	v_cndmask_b32_e32 v150, v150, v82, vcc
	v_cmp_eq_u32_e32 vcc, 3, v155
	v_lshrrev_b32_sdwa v160, v165, v159 dst_sel:DWORD dst_unused:UNUSED_PAD src0_sel:DWORD src1_sel:WORD_0
	v_lshrrev_b32_sdwa v161, v165, v159 dst_sel:DWORD dst_unused:UNUSED_PAD src0_sel:DWORD src1_sel:WORD_1
	v_cndmask_b32_e32 v163, v164, v15, vcc
	v_cndmask_b32_e32 v151, v151, v83, vcc
	ds_add_u32 v160, v162 offset:34416
	ds_add_u32 v161, v163 offset:34416
	s_waitcnt lgkmcnt(6)
	v_pk_add_f32 v[166:167], v[76:77], v[150:151] neg_lo:[0,1] neg_hi:[0,1]
	s_nop 0
	v_pk_fma_f32 v[166:167], v[166:167], v[166:167], v[6:7]
	v_pk_fma_f32 v[80:81], v[120:121], v[20:21], v[16:17] op_sel_hi:[1,0,0]
	v_pk_fma_f32 v[80:81], v[122:123], v[36:37], v[80:81] op_sel_hi:[1,0,1]
	s_nop 0
	v_exp_f32_e32 v82, v80
	v_exp_f32_e32 v83, v81
	v_cmp_eq_u32_e32 vcc, 1, v156
	v_cvt_pknorm_u16_f32 v158, v82, v83
	v_and_b32_e32 v159, s16, v158
	v_cndmask_b32_e32 v162, v164, v15, vcc
	v_cndmask_b32_e32 v152, v152, v82, vcc
	v_cmp_eq_u32_e32 vcc, 1, v157
	v_lshrrev_b32_sdwa v160, v165, v159 dst_sel:DWORD dst_unused:UNUSED_PAD src0_sel:DWORD src1_sel:WORD_0
	v_lshrrev_b32_sdwa v161, v165, v159 dst_sel:DWORD dst_unused:UNUSED_PAD src0_sel:DWORD src1_sel:WORD_1
	v_cndmask_b32_e32 v163, v164, v15, vcc
	v_cndmask_b32_e32 v153, v153, v83, vcc
	ds_add_u32 v160, v162 offset:1648
	ds_add_u32 v161, v163 offset:1648
	v_pk_fma_f32 v[80:81], v[120:121], v[20:21], v[16:17] op_sel:[0,1,1]
	v_pk_fma_f32 v[80:81], v[122:123], v[36:37], v[80:81] op_sel:[0,1,0]
	s_nop 0
	v_exp_f32_e32 v82, v80
	v_exp_f32_e32 v83, v81
	v_cmp_eq_u32_e32 vcc, 2, v156
	v_cvt_pknorm_u16_f32 v158, v82, v83
	v_and_b32_e32 v159, s16, v158
	v_cndmask_b32_e32 v162, v164, v15, vcc
	v_cndmask_b32_e32 v152, v152, v82, vcc
	v_cmp_eq_u32_e32 vcc, 2, v157
	v_lshrrev_b32_sdwa v160, v165, v159 dst_sel:DWORD dst_unused:UNUSED_PAD src0_sel:DWORD src1_sel:WORD_0
	v_lshrrev_b32_sdwa v161, v165, v159 dst_sel:DWORD dst_unused:UNUSED_PAD src0_sel:DWORD src1_sel:WORD_1
	v_cndmask_b32_e32 v163, v164, v15, vcc
	v_cndmask_b32_e32 v153, v153, v83, vcc
	ds_add_u32 v160, v162 offset:18032
	ds_add_u32 v161, v163 offset:18032
	v_pk_fma_f32 v[80:81], v[120:121], v[8:9], v[12:13] op_sel_hi:[1,0,0]
	v_pk_fma_f32 v[80:81], v[122:123], v[24:25], v[80:81] op_sel_hi:[1,0,1]
	s_nop 0
	v_exp_f32_e32 v82, v80
	v_exp_f32_e32 v83, v81
	v_cmp_eq_u32_e32 vcc, 3, v156
	v_cvt_pknorm_u16_f32 v158, v82, v83
	v_and_b32_e32 v159, s16, v158
	v_cndmask_b32_e32 v162, v164, v15, vcc
	v_cndmask_b32_e32 v152, v152, v82, vcc
	v_cmp_eq_u32_e32 vcc, 3, v157
	v_lshrrev_b32_sdwa v160, v165, v159 dst_sel:DWORD dst_unused:UNUSED_PAD src0_sel:DWORD src1_sel:WORD_0
	v_lshrrev_b32_sdwa v161, v165, v159 dst_sel:DWORD dst_unused:UNUSED_PAD src0_sel:DWORD src1_sel:WORD_1
	v_cndmask_b32_e32 v163, v164, v15, vcc
	v_cndmask_b32_e32 v153, v153, v83, vcc
	ds_add_u32 v160, v162 offset:34416
	ds_add_u32 v161, v163 offset:34416
	v_pk_add_f32 v[80:81], v[78:79], v[152:153] neg_lo:[0,1] neg_hi:[0,1]
	s_nop 0
	v_pk_fma_f32 v[6:7], v[80:81], v[80:81], v[166:167]
	ds_read_b128 v[76:79], v135
	v_mov_b32_e32 v164, 1
	v_mov_b32_e32 v165, 2
	v_mov_b32_e32 v150, 0
	v_mov_b32_e32 v151, 0
	v_mov_b32_e32 v152, 0
	v_mov_b32_e32 v153, 0
	v_and_b32_e32 v154, 3, v13
	v_bfe_u32 v155, v13, 2, 2
	v_bfe_u32 v156, v13, 4, 2
	v_bfe_u32 v157, v13, 6, 2
	s_mov_b32 s16, 0xfff0fff0
	v_pk_fma_f32 v[80:81], v[58:59], v[20:21], v[16:17] op_sel_hi:[1,0,0]
	v_pk_fma_f32 v[80:81], v[124:125], v[36:37], v[80:81] op_sel_hi:[1,0,1]
	s_nop 0
	v_exp_f32_e32 v82, v80
	v_exp_f32_e32 v83, v81
	v_cmp_eq_u32_e32 vcc, 1, v154
	v_cvt_pknorm_u16_f32 v158, v82, v83
	v_and_b32_e32 v159, s16, v158
	v_cndmask_b32_e32 v162, v164, v15, vcc
	v_cndmask_b32_e32 v150, v150, v82, vcc
	v_cmp_eq_u32_e32 vcc, 1, v155
	v_lshrrev_b32_sdwa v160, v165, v159 dst_sel:DWORD dst_unused:UNUSED_PAD src0_sel:DWORD src1_sel:WORD_0
	v_lshrrev_b32_sdwa v161, v165, v159 dst_sel:DWORD dst_unused:UNUSED_PAD src0_sel:DWORD src1_sel:WORD_1
	v_cndmask_b32_e32 v163, v164, v15, vcc
	v_cndmask_b32_e32 v151, v151, v83, vcc
	ds_add_u32 v160, v162 offset:1648
	ds_add_u32 v161, v163 offset:1648
	v_pk_fma_f32 v[80:81], v[58:59], v[20:21], v[16:17] op_sel:[0,1,1]
	v_pk_fma_f32 v[80:81], v[124:125], v[36:37], v[80:81] op_sel:[0,1,0]
	s_nop 0
	v_exp_f32_e32 v82, v80
	v_exp_f32_e32 v83, v81
	v_cmp_eq_u32_e32 vcc, 2, v154
	v_cvt_pknorm_u16_f32 v158, v82, v83
	v_and_b32_e32 v159, s16, v158
	v_cndmask_b32_e32 v162, v164, v15, vcc
	v_cndmask_b32_e32 v150, v150, v82, vcc
	v_cmp_eq_u32_e32 vcc, 2, v155
	v_lshrrev_b32_sdwa v160, v165, v159 dst_sel:DWORD dst_unused:UNUSED_PAD src0_sel:DWORD src1_sel:WORD_0
	v_lshrrev_b32_sdwa v161, v165, v159 dst_sel:DWORD dst_unused:UNUSED_PAD src0_sel:DWORD src1_sel:WORD_1
	v_cndmask_b32_e32 v163, v164, v15, vcc
	v_cndmask_b32_e32 v151, v151, v83, vcc
	ds_add_u32 v160, v162 offset:18032
	ds_add_u32 v161, v163 offset:18032
	v_pk_fma_f32 v[80:81], v[58:59], v[8:9], v[12:13] op_sel_hi:[1,0,0]
	v_pk_fma_f32 v[80:81], v[124:125], v[24:25], v[80:81] op_sel_hi:[1,0,1]
	s_nop 0
	v_exp_f32_e32 v82, v80
	v_exp_f32_e32 v83, v81
	v_cmp_eq_u32_e32 vcc, 3, v154
	v_cvt_pknorm_u16_f32 v158, v82, v83
	v_and_b32_e32 v159, s16, v158
	v_cndmask_b32_e32 v162, v164, v15, vcc
	v_cndmask_b32_e32 v150, v150, v82, vcc
	v_cmp_eq_u32_e32 vcc, 3, v155
	v_lshrrev_b32_sdwa v160, v165, v159 dst_sel:DWORD dst_unused:UNUSED_PAD src0_sel:DWORD src1_sel:WORD_0
	v_lshrrev_b32_sdwa v161, v165, v159 dst_sel:DWORD dst_unused:UNUSED_PAD src0_sel:DWORD src1_sel:WORD_1
	v_cndmask_b32_e32 v163, v164, v15, vcc
	v_cndmask_b32_e32 v151, v151, v83, vcc
	ds_add_u32 v160, v162 offset:34416
	ds_add_u32 v161, v163 offset:34416
	s_waitcnt lgkmcnt(6)
	v_pk_add_f32 v[166:167], v[76:77], v[150:151] neg_lo:[0,1] neg_hi:[0,1]
	s_nop 0
	v_pk_fma_f32 v[166:167], v[166:167], v[166:167], v[6:7]
	v_pk_fma_f32 v[80:81], v[60:61], v[20:21], v[16:17] op_sel_hi:[1,0,0]
	v_pk_fma_f32 v[80:81], v[126:127], v[36:37], v[80:81] op_sel_hi:[1,0,1]
	s_nop 0
	v_exp_f32_e32 v82, v80
	v_exp_f32_e32 v83, v81
	v_cmp_eq_u32_e32 vcc, 1, v156
	v_cvt_pknorm_u16_f32 v158, v82, v83
	v_and_b32_e32 v159, s16, v158
	v_cndmask_b32_e32 v162, v164, v15, vcc
	v_cndmask_b32_e32 v152, v152, v82, vcc
	v_cmp_eq_u32_e32 vcc, 1, v157
	v_lshrrev_b32_sdwa v160, v165, v159 dst_sel:DWORD dst_unused:UNUSED_PAD src0_sel:DWORD src1_sel:WORD_0
	v_lshrrev_b32_sdwa v161, v165, v159 dst_sel:DWORD dst_unused:UNUSED_PAD src0_sel:DWORD src1_sel:WORD_1
	v_cndmask_b32_e32 v163, v164, v15, vcc
	v_cndmask_b32_e32 v153, v153, v83, vcc
	ds_add_u32 v160, v162 offset:1648
	ds_add_u32 v161, v163 offset:1648
	v_pk_fma_f32 v[80:81], v[60:61], v[20:21], v[16:17] op_sel:[0,1,1]
	v_pk_fma_f32 v[80:81], v[126:127], v[36:37], v[80:81] op_sel:[0,1,0]
	s_nop 0
	v_exp_f32_e32 v82, v80
	v_exp_f32_e32 v83, v81
	v_cmp_eq_u32_e32 vcc, 2, v156
	v_cvt_pknorm_u16_f32 v158, v82, v83
	v_and_b32_e32 v159, s16, v158
	v_cndmask_b32_e32 v162, v164, v15, vcc
	v_cndmask_b32_e32 v152, v152, v82, vcc
	v_cmp_eq_u32_e32 vcc, 2, v157
	v_lshrrev_b32_sdwa v160, v165, v159 dst_sel:DWORD dst_unused:UNUSED_PAD src0_sel:DWORD src1_sel:WORD_0
	v_lshrrev_b32_sdwa v161, v165, v159 dst_sel:DWORD dst_unused:UNUSED_PAD src0_sel:DWORD src1_sel:WORD_1
	v_cndmask_b32_e32 v163, v164, v15, vcc
	v_cndmask_b32_e32 v153, v153, v83, vcc
	ds_add_u32 v160, v162 offset:18032
	ds_add_u32 v161, v163 offset:18032
	v_pk_fma_f32 v[80:81], v[60:61], v[8:9], v[12:13] op_sel_hi:[1,0,0]
	v_pk_fma_f32 v[80:81], v[126:127], v[24:25], v[80:81] op_sel_hi:[1,0,1]
	s_nop 0
	v_exp_f32_e32 v82, v80
	v_exp_f32_e32 v83, v81
	v_cmp_eq_u32_e32 vcc, 3, v156
	v_cvt_pknorm_u16_f32 v158, v82, v83
	v_and_b32_e32 v159, s16, v158
	v_cndmask_b32_e32 v162, v164, v15, vcc
	v_cndmask_b32_e32 v152, v152, v82, vcc
	v_cmp_eq_u32_e32 vcc, 3, v157
	v_lshrrev_b32_sdwa v160, v165, v159 dst_sel:DWORD dst_unused:UNUSED_PAD src0_sel:DWORD src1_sel:WORD_0
	v_lshrrev_b32_sdwa v161, v165, v159 dst_sel:DWORD dst_unused:UNUSED_PAD src0_sel:DWORD src1_sel:WORD_1
	v_cndmask_b32_e32 v163, v164, v15, vcc
	v_cndmask_b32_e32 v153, v153, v83, vcc
	ds_add_u32 v160, v162 offset:34416
	ds_add_u32 v161, v163 offset:34416
	v_pk_add_f32 v[80:81], v[78:79], v[152:153] neg_lo:[0,1] neg_hi:[0,1]
	s_nop 0
	v_pk_fma_f32 v[6:7], v[80:81], v[80:81], v[166:167]
	ds_read_b128 v[76:79], v70
	v_mov_b32_e32 v164, 1
	v_mov_b32_e32 v165, 2
	v_mov_b32_e32 v150, 0
	v_mov_b32_e32 v151, 0
	v_mov_b32_e32 v152, 0
	v_mov_b32_e32 v153, 0
	v_and_b32_e32 v154, 3, v9
	v_bfe_u32 v155, v9, 2, 2
	v_bfe_u32 v156, v9, 4, 2
	v_bfe_u32 v157, v9, 6, 2
	s_mov_b32 s16, 0xfff0fff0
	v_pk_fma_f32 v[80:81], v[62:63], v[20:21], v[16:17] op_sel_hi:[1,0,0]
	v_pk_fma_f32 v[80:81], v[66:67], v[36:37], v[80:81] op_sel_hi:[1,0,1]
	s_nop 0
	v_exp_f32_e32 v82, v80
	v_exp_f32_e32 v83, v81
	v_cmp_eq_u32_e32 vcc, 1, v154
	v_cvt_pknorm_u16_f32 v158, v82, v83
	v_and_b32_e32 v159, s16, v158
	v_cndmask_b32_e32 v162, v164, v15, vcc
	v_cndmask_b32_e32 v150, v150, v82, vcc
	v_cmp_eq_u32_e32 vcc, 1, v155
	v_lshrrev_b32_sdwa v160, v165, v159 dst_sel:DWORD dst_unused:UNUSED_PAD src0_sel:DWORD src1_sel:WORD_0
	v_lshrrev_b32_sdwa v161, v165, v159 dst_sel:DWORD dst_unused:UNUSED_PAD src0_sel:DWORD src1_sel:WORD_1
	v_cndmask_b32_e32 v163, v164, v15, vcc
	v_cndmask_b32_e32 v151, v151, v83, vcc
	ds_add_u32 v160, v162 offset:1648
	ds_add_u32 v161, v163 offset:1648
	v_pk_fma_f32 v[80:81], v[62:63], v[20:21], v[16:17] op_sel:[0,1,1]
	v_pk_fma_f32 v[80:81], v[66:67], v[36:37], v[80:81] op_sel:[0,1,0]
	s_nop 0
	v_exp_f32_e32 v82, v80
	v_exp_f32_e32 v83, v81
	v_cmp_eq_u32_e32 vcc, 2, v154
	v_cvt_pknorm_u16_f32 v158, v82, v83
	v_and_b32_e32 v159, s16, v158
	v_cndmask_b32_e32 v162, v164, v15, vcc
	v_cndmask_b32_e32 v150, v150, v82, vcc
	v_cmp_eq_u32_e32 vcc, 2, v155
	v_lshrrev_b32_sdwa v160, v165, v159 dst_sel:DWORD dst_unused:UNUSED_PAD src0_sel:DWORD src1_sel:WORD_0
	v_lshrrev_b32_sdwa v161, v165, v159 dst_sel:DWORD dst_unused:UNUSED_PAD src0_sel:DWORD src1_sel:WORD_1
	v_cndmask_b32_e32 v163, v164, v15, vcc
	v_cndmask_b32_e32 v151, v151, v83, vcc
	ds_add_u32 v160, v162 offset:18032
	ds_add_u32 v161, v163 offset:18032
	v_pk_fma_f32 v[80:81], v[62:63], v[8:9], v[12:13] op_sel_hi:[1,0,0]
	v_pk_fma_f32 v[80:81], v[66:67], v[24:25], v[80:81] op_sel_hi:[1,0,1]
	s_nop 0
	v_exp_f32_e32 v82, v80
	v_exp_f32_e32 v83, v81
	v_cmp_eq_u32_e32 vcc, 3, v154
	v_cvt_pknorm_u16_f32 v158, v82, v83
	v_and_b32_e32 v159, s16, v158
	v_cndmask_b32_e32 v162, v164, v15, vcc
	v_cndmask_b32_e32 v150, v150, v82, vcc
	v_cmp_eq_u32_e32 vcc, 3, v155
	v_lshrrev_b32_sdwa v160, v165, v159 dst_sel:DWORD dst_unused:UNUSED_PAD src0_sel:DWORD src1_sel:WORD_0
	v_lshrrev_b32_sdwa v161, v165, v159 dst_sel:DWORD dst_unused:UNUSED_PAD src0_sel:DWORD src1_sel:WORD_1
	v_cndmask_b32_e32 v163, v164, v15, vcc
	v_cndmask_b32_e32 v151, v151, v83, vcc
	ds_add_u32 v160, v162 offset:34416
	ds_add_u32 v161, v163 offset:34416
	s_waitcnt lgkmcnt(6)
	v_pk_add_f32 v[166:167], v[76:77], v[150:151] neg_lo:[0,1] neg_hi:[0,1]
	s_nop 0
	v_pk_fma_f32 v[166:167], v[166:167], v[166:167], v[6:7]
	v_pk_fma_f32 v[80:81], v[64:65], v[20:21], v[16:17] op_sel_hi:[1,0,0]
	v_pk_fma_f32 v[80:81], v[68:69], v[36:37], v[80:81] op_sel_hi:[1,0,1]
	s_nop 0
	v_exp_f32_e32 v82, v80
	v_exp_f32_e32 v83, v81
	v_cmp_eq_u32_e32 vcc, 1, v156
	v_cvt_pknorm_u16_f32 v158, v82, v83
	v_and_b32_e32 v159, s16, v158
	v_cndmask_b32_e32 v162, v164, v15, vcc
	v_cndmask_b32_e32 v152, v152, v82, vcc
	v_cmp_eq_u32_e32 vcc, 1, v157
	v_lshrrev_b32_sdwa v160, v165, v159 dst_sel:DWORD dst_unused:UNUSED_PAD src0_sel:DWORD src1_sel:WORD_0
	v_lshrrev_b32_sdwa v161, v165, v159 dst_sel:DWORD dst_unused:UNUSED_PAD src0_sel:DWORD src1_sel:WORD_1
	v_cndmask_b32_e32 v163, v164, v15, vcc
	v_cndmask_b32_e32 v153, v153, v83, vcc
	ds_add_u32 v160, v162 offset:1648
	ds_add_u32 v161, v163 offset:1648
	v_pk_fma_f32 v[80:81], v[64:65], v[20:21], v[16:17] op_sel:[0,1,1]
	v_pk_fma_f32 v[80:81], v[68:69], v[36:37], v[80:81] op_sel:[0,1,0]
	s_nop 0
	v_exp_f32_e32 v82, v80
	v_exp_f32_e32 v83, v81
	v_cmp_eq_u32_e32 vcc, 2, v156
	v_cvt_pknorm_u16_f32 v158, v82, v83
	v_and_b32_e32 v159, s16, v158
	v_cndmask_b32_e32 v162, v164, v15, vcc
	v_cndmask_b32_e32 v152, v152, v82, vcc
	v_cmp_eq_u32_e32 vcc, 2, v157
	v_lshrrev_b32_sdwa v160, v165, v159 dst_sel:DWORD dst_unused:UNUSED_PAD src0_sel:DWORD src1_sel:WORD_0
	v_lshrrev_b32_sdwa v161, v165, v159 dst_sel:DWORD dst_unused:UNUSED_PAD src0_sel:DWORD src1_sel:WORD_1
	v_cndmask_b32_e32 v163, v164, v15, vcc
	v_cndmask_b32_e32 v153, v153, v83, vcc
	ds_add_u32 v160, v162 offset:18032
	ds_add_u32 v161, v163 offset:18032
	v_pk_fma_f32 v[80:81], v[64:65], v[8:9], v[12:13] op_sel_hi:[1,0,0]
	v_pk_fma_f32 v[80:81], v[68:69], v[24:25], v[80:81] op_sel_hi:[1,0,1]
	s_nop 0
	v_exp_f32_e32 v82, v80
	v_exp_f32_e32 v83, v81
	v_cmp_eq_u32_e32 vcc, 3, v156
	v_cvt_pknorm_u16_f32 v158, v82, v83
	v_and_b32_e32 v159, s16, v158
	v_cndmask_b32_e32 v162, v164, v15, vcc
	v_cndmask_b32_e32 v152, v152, v82, vcc
	v_cmp_eq_u32_e32 vcc, 3, v157
	v_lshrrev_b32_sdwa v160, v165, v159 dst_sel:DWORD dst_unused:UNUSED_PAD src0_sel:DWORD src1_sel:WORD_0
	v_lshrrev_b32_sdwa v161, v165, v159 dst_sel:DWORD dst_unused:UNUSED_PAD src0_sel:DWORD src1_sel:WORD_1
	v_cndmask_b32_e32 v163, v164, v15, vcc
	v_cndmask_b32_e32 v153, v153, v83, vcc
	ds_add_u32 v160, v162 offset:34416
	ds_add_u32 v161, v163 offset:34416
	v_pk_add_f32 v[80:81], v[78:79], v[152:153] neg_lo:[0,1] neg_hi:[0,1]
	s_nop 0
	v_pk_fma_f32 v[6:7], v[80:81], v[80:81], v[166:167]
	s_and_saveexec_b64 s[8:9], s[4:5]
	s_cbranch_execz .LBB0_60
	v_mov_b32_e32 v22, v20
	v_mov_b32_e32 v23, v20
	v_mov_b32_e32 v24, v16
	v_mov_b32_e32 v25, v16
	v_mov_b32_e32 v18, v36
	v_mov_b32_e32 v19, v36
	v_pk_fma_f32 v[2:3], v[54:55], v[22:23], v[24:25]
	v_add_u32_e32 v1, 0x18000, v1
	v_pk_fma_f32 v[2:3], v[50:51], v[18:19], v[2:3]
	v_bfe_u32 v30, v40, 2, 2
	v_exp_f32_e32 v10, v2
	v_exp_f32_e32 v14, v3
	ds_read_b128 v[2:5], v1
	v_and_b32_e32 v1, 3, v40
	v_cmp_eq_u32_e32 vcc, 1, v1
	v_cvt_pknorm_u16_f32 v28, v10, v14
	v_lshrrev_b32_e32 v29, 4, v28
	v_bfe_u32 v31, v28, 4, 12
	v_bitop3_b32 v29, v29, s3, v29 bitop3:0xc
	v_mov_b32_e32 v29, v31
	v_lshl_add_u32 v29, v29, 2, v11
	v_cndmask_b32_e32 v31, 1, v15, vcc
	v_lshrrev_b32_e32 v28, 20, v28
	ds_add_u32 v29, v31
	v_cndmask_b32_e32 v10, 0, v10, vcc
	v_xor_b32_e32 v29, 0xfff, v28
	v_cmp_eq_u32_e32 vcc, 1, v30
	v_mov_b32_e32 v20, v21
	v_mov_b32_e32 v16, v17
	v_mov_b32_e32 v28, v28
	v_mov_b32_e32 v36, v37
	v_lshl_add_u32 v31, v28, 2, v11
	v_pk_fma_f32 v[28:29], v[54:55], v[20:21], v[16:17]
	v_cndmask_b32_e32 v14, 0, v14, vcc
	v_pk_fma_f32 v[28:29], v[50:51], v[36:37], v[28:29]
	v_mov_b32_e32 v9, v8
	v_exp_f32_e32 v28, v28
	v_exp_f32_e32 v32, v29
	v_cndmask_b32_e32 v29, 1, v15, vcc
	ds_add_u32 v31, v29
	v_cmp_eq_u32_e32 vcc, 2, v1
	v_cvt_pknorm_u16_f32 v29, v28, v32
	v_lshrrev_b32_e32 v31, 4, v29
	v_bfe_u32 v33, v29, 4, 12
	v_bitop3_b32 v31, v31, s3, v31 bitop3:0xc
	v_cndmask_b32_e32 v10, v10, v28, vcc
	v_lshrrev_b32_e32 v28, 20, v29
	v_mov_b32_e32 v31, v33
	v_cndmask_b32_e32 v33, 1, v15, vcc
	v_xor_b32_e32 v29, 0xfff, v28
	v_cmp_eq_u32_e32 vcc, 2, v30
	v_mov_b32_e32 v13, v12
	v_lshl_add_u32 v31, v31, 2, v11
	v_mov_b32_e32 v28, v28
	v_mov_b32_e32 v26, v38
	v_mov_b32_e32 v27, v38
	ds_add_u32 v31, v33 offset:16384
	v_lshl_add_u32 v31, v28, 2, v11
	v_pk_fma_f32 v[28:29], v[54:55], v[8:9], v[12:13]
	v_cndmask_b32_e32 v33, 1, v15, vcc
	v_pk_fma_f32 v[28:29], v[50:51], v[26:27], v[28:29]
	ds_add_u32 v31, v33 offset:16384
	v_exp_f32_e32 v28, v28
	v_exp_f32_e32 v29, v29
	v_cndmask_b32_e32 v14, v14, v32, vcc
	v_cmp_eq_u32_e32 vcc, 3, v1
	v_pk_fma_f32 v[22:23], v[22:23], v[46:47], v[24:25]
	v_cvt_pknorm_u16_f32 v31, v28, v29
	v_lshrrev_b32_e32 v32, 4, v31
	v_bfe_u32 v33, v31, 4, 12
	v_bitop3_b32 v32, v32, s3, v32 bitop3:0xc
	v_mov_b32_e32 v1, v33
	v_lshl_add_u32 v1, v1, 2, v11
	v_cndmask_b32_e32 v32, 1, v15, vcc
	ds_add_u32 v1, v32 offset:32768
	v_lshrrev_b32_e32 v1, 20, v31
	v_cndmask_b32_e32 v28, v10, v28, vcc
	v_xor_b32_e32 v10, 0xfff, v1
	v_cmp_eq_u32_e32 vcc, 3, v30
	v_pk_fma_f32 v[18:19], v[18:19], v[74:75], v[22:23]
	s_nop 0
	v_mov_b32_e32 v1, v1
	v_lshl_add_u32 v1, v1, 2, v11
	v_cndmask_b32_e32 v10, 1, v15, vcc
	ds_add_u32 v1, v10 offset:32768
	v_exp_f32_e32 v1, v18
	v_exp_f32_e32 v10, v19
	v_cndmask_b32_e32 v29, v14, v29, vcc
	s_waitcnt lgkmcnt(6)
	v_pk_add_f32 v[2:3], v[2:3], v[28:29] neg_lo:[0,1] neg_hi:[0,1]
	v_bfe_u32 v14, v40, 4, 2
	v_pk_fma_f32 v[2:3], v[2:3], v[2:3], v[6:7]
	v_cvt_pknorm_u16_f32 v6, v1, v10
	v_lshrrev_b32_e32 v7, 4, v6
	v_bfe_u32 v19, v6, 4, 12
	v_bitop3_b32 v7, v7, s3, v7 bitop3:0xc
	v_cmp_eq_u32_e32 vcc, 1, v14
	v_bfe_u32 v18, v40, 6, 2
	v_lshrrev_b32_e32 v6, 20, v6
	v_mov_b32_e32 v7, v19
	v_lshl_add_u32 v7, v7, 2, v11
	v_cndmask_b32_e32 v19, 1, v15, vcc
	ds_add_u32 v7, v19
	v_cndmask_b32_e32 v1, 0, v1, vcc
	v_xor_b32_e32 v7, 0xfff, v6
	v_cmp_eq_u32_e32 vcc, 1, v18
	v_cmp_eq_u32_e64 s[4:5], 3, v18
	s_nop 0
	v_mov_b32_e32 v6, v6
	v_lshl_add_u32 v19, v6, 2, v11
	v_pk_fma_f32 v[6:7], v[20:21], v[46:47], v[16:17]
	v_cndmask_b32_e32 v10, 0, v10, vcc
	v_pk_fma_f32 v[6:7], v[36:37], v[74:75], v[6:7]
	s_nop 0
	v_exp_f32_e32 v6, v6
	v_exp_f32_e32 v16, v7
	v_cndmask_b32_e32 v7, 1, v15, vcc
	ds_add_u32 v19, v7
	v_cmp_eq_u32_e32 vcc, 2, v14
	v_cvt_pknorm_u16_f32 v7, v6, v16
	v_lshrrev_b32_e32 v17, 4, v7
	v_bfe_u32 v19, v7, 4, 12
	v_bitop3_b32 v17, v17, s3, v17 bitop3:0xc
	v_cndmask_b32_e32 v1, v1, v6, vcc
	v_lshrrev_b32_e32 v6, 20, v7
	v_mov_b32_e32 v17, v19
	v_cndmask_b32_e32 v19, 1, v15, vcc
	v_xor_b32_e32 v7, 0xfff, v6
	v_cmp_eq_u32_e32 vcc, 2, v18
	v_lshl_add_u32 v17, v17, 2, v11
	ds_add_u32 v17, v19 offset:16384
	v_mov_b32_e32 v6, v6
	v_lshl_add_u32 v17, v6, 2, v11
	v_pk_fma_f32 v[6:7], v[8:9], v[46:47], v[12:13]
	v_cndmask_b32_e32 v8, 1, v15, vcc
	v_pk_fma_f32 v[6:7], v[26:27], v[74:75], v[6:7]
	ds_add_u32 v17, v8 offset:16384
	v_exp_f32_e32 v6, v6
	v_exp_f32_e32 v7, v7
	v_cndmask_b32_e32 v8, v10, v16, vcc
	v_cmp_eq_u32_e32 vcc, 3, v14
	v_cvt_pknorm_u16_f32 v9, v6, v7
	v_lshrrev_b32_e32 v10, 4, v9
	v_bfe_u32 v12, v9, 4, 12
	v_bitop3_b32 v10, v10, s3, v10 bitop3:0xc
	v_mov_b32_e32 v10, v12
	v_lshl_add_u32 v10, v10, 2, v11
	v_cndmask_b32_e32 v12, 1, v15, vcc
	v_lshrrev_b32_e32 v9, 20, v9
	ds_add_u32 v10, v12 offset:32768
	v_xor_b32_e32 v10, 0xfff, v9
	v_mov_b32_e32 v9, v9
	v_lshl_add_u32 v9, v9, 2, v11
	v_cndmask_b32_e64 v10, 1, v15, s[4:5]
	ds_add_u32 v9, v10 offset:32768
	v_cndmask_b32_e32 v6, v1, v6, vcc
	v_cndmask_b32_e64 v7, v8, v7, s[4:5]
	v_pk_add_f32 v[4:5], v[4:5], v[6:7] neg_lo:[0,1] neg_hi:[0,1]
	s_nop 0
	v_pk_fma_f32 v[6:7], v[4:5], v[4:5], v[2:3]

_Z8k5_finalPK15HIP_vector_typeIjLj2EEPKfS4_PyPf:
	s_load_dwordx2 s[4:5], s[0:1], 0x0
	s_load_dwordx4 s[8:11], s[0:1], 0x18
	s_ashr_i32 s3, s2, 31
	s_lshl_b64 s[6:7], s[2:3], 15
	v_lshlrev_b32_e32 v1, 5, v0
	s_waitcnt lgkmcnt(0)
	s_add_u32 s4, s4, s6
	s_addc_u32 s5, s5, s7
	global_load_dwordx4 v[6:9], v1, s[4:5] offset:16
	global_load_dwordx4 v[2:5], v1, s[4:5]
	v_sub_u32_e32 v42, 0x7fe0, v1
	global_load_dwordx4 v[34:37], v42, s[4:5]
	global_load_dwordx4 v[38:41], v42, s[4:5] offset:16
	s_cmp_eq_u32 s2, 0
	s_cselect_b64 s[6:7], -1, 0
	s_cmp_lg_u32 s2, 0
	v_mov_b32_e32 v1, 0
	s_cbranch_scc1 .LBB4_6
	s_movk_i32 s2, 0x100
	v_cmp_gt_u32_e32 vcc, s2, v0
	v_mov_b32_e32 v1, 0
	s_and_saveexec_b64 s[2:3], vcc
	s_cbranch_execz .LBB4_3
	s_load_dwordx2 s[4:5], s[0:1], 0x10
	v_lshlrev_b32_e32 v1, 2, v0
	s_waitcnt lgkmcnt(0)
	global_load_dword v1, v1, s[4:5]

.LBB4_6:
	s_waitcnt vmcnt(0)
	v_mov_b32_e32 v2, v40
	v_mov_b32_e32 v4, v38
	v_mov_b32_e32 v6, v36
	v_mov_b32_e32 v8, v34
	v_add_u32_e32 v12, v5, v3
	v_add3_u32 v28, v12, v7, v9
	v_add_u32_e32 v11, v4, v2
	v_add3_u32 v29, v11, v6, v8
	v_mbcnt_lo_u32_b32 v12, -1, 0
	v_mbcnt_hi_u32_b32 v26, -1, v12
	v_and_b32_e32 v10, 63, v0
	v_lshrrev_b32_e32 v27, 6, v0
	v_cmp_eq_u32_e64 s[2:3], 0, v10
	v_mov_b32_e32 v30, v28
	v_mov_b32_e32 v31, v29
	s_nop 0
	v_add_u32_dpp v30, v30, v30 row_shl:1 row_mask:0xf bank_mask:0xf bound_ctrl:1
	v_add_u32_dpp v31, v31, v31 row_shl:1 row_mask:0xf bank_mask:0xf bound_ctrl:1
	s_nop 0
	v_add_u32_dpp v30, v30, v30 row_shl:2 row_mask:0xf bank_mask:0xf bound_ctrl:1
	v_add_u32_dpp v31, v31, v31 row_shl:2 row_mask:0xf bank_mask:0xf bound_ctrl:1
	s_nop 0
	v_add_u32_dpp v30, v30, v30 row_shl:4 row_mask:0xf bank_mask:0xf bound_ctrl:1
	v_add_u32_dpp v31, v31, v31 row_shl:4 row_mask:0xf bank_mask:0xf bound_ctrl:1
	s_nop 0
	v_add_u32_dpp v30, v30, v30 row_shl:8 row_mask:0xf bank_mask:0xf bound_ctrl:1
	v_add_u32_dpp v31, v31, v31 row_shl:8 row_mask:0xf bank_mask:0xf bound_ctrl:1
	s_nop 0
	v_readlane_b32 s12, v30, 16
	v_readlane_b32 s13, v30, 32
	v_readlane_b32 s14, v30, 48
	v_readlane_b32 s15, v31, 16
	v_readlane_b32 s16, v31, 32
	v_readlane_b32 s17, v31, 48
	s_add_u32 s13, s13, s14
	s_add_u32 s12, s12, s13
	s_add_u32 s16, s16, s17
	s_add_u32 s15, s15, s16
	v_mov_b32_e32 v12, s14
	v_mov_b32_e32 v13, s13
	v_mov_b32_e32 v14, s12
	v_mov_b32_e32 v15, s17
	v_mov_b32_e32 v16, s16
	v_mov_b32_e32 v17, s15
	s_nop 0
	v_add_u32_dpp v30, v12, v30 quad_perm:[0,1,2,3] row_mask:0x4 bank_mask:0xf
	v_add_u32_dpp v31, v15, v31 quad_perm:[0,1,2,3] row_mask:0x4 bank_mask:0xf
	v_add_u32_dpp v30, v13, v30 quad_perm:[0,1,2,3] row_mask:0x2 bank_mask:0xf
	v_add_u32_dpp v31, v16, v31 quad_perm:[0,1,2,3] row_mask:0x2 bank_mask:0xf
	v_add_u32_dpp v30, v14, v30 quad_perm:[0,1,2,3] row_mask:0x1 bank_mask:0xf
	v_add_u32_dpp v31, v17, v31 quad_perm:[0,1,2,3] row_mask:0x1 bank_mask:0xf
	s_and_saveexec_b64 s[4:5], s[2:3]
	v_lshlrev_b32_e32 v10, 2, v27
	v_add_u32_e32 v10, 0x3000, v10
	ds_write2_b32 v10, v30, v31 offset0:32 offset1:48
	s_or_b64 exec, exec, s[4:5]
	v_mov_b32_e32 v10, 0
	s_waitcnt lgkmcnt(0)
	s_barrier
	v_sub_u32_e32 v29, v31, v29
	v_sub_u32_e32 v28, v30, v28
	v_and_b32_e32 v32, 15, v26
	v_lshlrev_b32_e32 v33, 2, v32
	ds_read_b32 v30, v33 offset:12480
	ds_read_b32 v31, v33 offset:12416
	v_cmp_gt_u32_e32 vcc, v32, v27
	s_waitcnt lgkmcnt(0)
	s_nop 0
	v_cndmask_b32_e32 v34, 0, v30, vcc
	v_cndmask_b32_e32 v35, 0, v31, vcc
	s_nop 0
	v_add_u32_dpp v30, v30, v30 row_ror:8 row_mask:0xf bank_mask:0xf bound_ctrl:1
	v_add_u32_dpp v34, v34, v34 row_ror:8 row_mask:0xf bank_mask:0xf bound_ctrl:1
	v_add_u32_dpp v35, v35, v35 row_ror:8 row_mask:0xf bank_mask:0xf bound_ctrl:1
	v_add_u32_dpp v30, v30, v30 row_ror:4 row_mask:0xf bank_mask:0xf bound_ctrl:1
	v_add_u32_dpp v34, v34, v34 row_ror:4 row_mask:0xf bank_mask:0xf bound_ctrl:1
	v_add_u32_dpp v35, v35, v35 row_ror:4 row_mask:0xf bank_mask:0xf bound_ctrl:1
	v_add_u32_dpp v30, v30, v30 row_ror:2 row_mask:0xf bank_mask:0xf bound_ctrl:1
	v_add_u32_dpp v34, v34, v34 row_ror:2 row_mask:0xf bank_mask:0xf bound_ctrl:1
	v_add_u32_dpp v35, v35, v35 row_ror:2 row_mask:0xf bank_mask:0xf bound_ctrl:1
	v_add_u32_dpp v30, v30, v30 row_ror:1 row_mask:0xf bank_mask:0xf bound_ctrl:1
	v_add_u32_dpp v34, v34, v34 row_ror:1 row_mask:0xf bank_mask:0xf bound_ctrl:1
	v_add_u32_dpp v35, v35, v35 row_ror:1 row_mask:0xf bank_mask:0xf bound_ctrl:1
	v_add_u32_e32 v29, v29, v34
	v_add_u32_e32 v28, v28, v35
	v_mov_b32_e32 v10, v30
	v_add_u32_e32 v11, v28, v9
	v_cvt_f32_u32_e32 v9, v11
	v_cvt_f32_u32_e32 v10, v10
	v_add_u32_e32 v12, v29, v8
	v_mov_b32_e32 v8, 0
	v_add_f32_e32 v13, v10, v9
	v_cmp_lt_f32_e32 vcc, 0, v13
	v_mov_b32_e32 v9, 0
	s_and_saveexec_b64 s[4:5], vcc
	s_cbranch_execz .LBB4_14
	v_add_u32_e32 v9, v12, v11
	v_cvt_f32_u32_e32 v9, v9
	v_div_scale_f32 v14, s[12:13], v13, v13, v9
	v_rcp_f32_e32 v15, v14
	v_div_scale_f32 v16, vcc, v9, v13, v9
	v_fma_f32 v17, -v14, v15, 1.0
	v_fmac_f32_e32 v15, v17, v15
	v_mul_f32_e32 v17, v16, v15
	v_fma_f32 v18, -v14, v17, v16
	v_fmac_f32_e32 v17, v18, v15
	v_fma_f32 v14, -v14, v17, v16
	v_div_fmas_f32 v14, v14, v15, v17
	v_div_fixup_f32 v9, v14, v13, v9

	.amdhsa_kernel _Z8k5_finalPK15HIP_vector_typeIjLj2EEPKfS4_PyPf
		.amdhsa_group_segment_fixed_size 12544
		.amdhsa_private_segment_fixed_size 0
		.amdhsa_kernarg_size 296
		.amdhsa_user_sgpr_count 2
		.amdhsa_user_sgpr_dispatch_ptr 0
		.amdhsa_user_sgpr_queue_ptr 0
		.amdhsa_user_sgpr_kernarg_segment_ptr 1
		.amdhsa_user_sgpr_dispatch_id 0
		.amdhsa_user_sgpr_kernarg_preload_length 0
		.amdhsa_user_sgpr_kernarg_preload_offset 0
		.amdhsa_user_sgpr_private_segment_size 0
		.amdhsa_uses_dynamic_stack 0
		.amdhsa_enable_private_segment 0
		.amdhsa_system_sgpr_workgroup_id_x 1
		.amdhsa_system_sgpr_workgroup_id_y 0
		.amdhsa_system_sgpr_workgroup_id_z 0
		.amdhsa_system_sgpr_workgroup_info 0
		.amdhsa_system_vgpr_workitem_id 0
		.amdhsa_next_free_vgpr 44
		.amdhsa_next_free_sgpr 24
		.amdhsa_accum_offset 44
		.amdhsa_reserve_vcc 1
		.amdhsa_float_round_mode_32 0
		.amdhsa_float_round_mode_16_64 0
		.amdhsa_float_denorm_mode_32 3
		.amdhsa_float_denorm_mode_16_64 3
		.amdhsa_dx10_clamp 1
		.amdhsa_ieee_mode 1
		.amdhsa_fp16_overflow 0
		.amdhsa_tg_split 0
		.amdhsa_exception_fp_ieee_invalid_op 0
		.amdhsa_exception_fp_denorm_src 0
		.amdhsa_exception_fp_ieee_div_zero 0
		.amdhsa_exception_fp_ieee_overflow 0
		.amdhsa_exception_fp_ieee_underflow 0
		.amdhsa_exception_fp_ieee_inexact 0
		.amdhsa_exception_int_div_zero 0
	.end_amdhsa_kernel

amdhsa.kernels:
  - .agpr_count:     0
    .args:
      - .actual_access:  read_only
        .address_space:  global
        .offset:         0
        .size:           8
        .value_kind:     global_buffer
      - .actual_access:  read_only
        .address_space:  global
        .offset:         8
        .size:           8
        .value_kind:     global_buffer
      - .address_space:  global
        .offset:         16
        .size:           8
        .value_kind:     global_buffer
      - .actual_access:  write_only
        .address_space:  global
        .offset:         24
        .size:           8
        .value_kind:     global_buffer
      - .actual_access:  write_only
        .address_space:  global
        .offset:         32
        .size:           8
        .value_kind:     global_buffer
      - .address_space:  global
        .offset:         40
        .size:           8
        .value_kind:     global_buffer
    .group_segment_fixed_size: 1648
    .kernarg_segment_align: 8
    .kernarg_segment_size: 48
    .language:       OpenCL C
    .language_version:
      - 2
      - 0
    .max_flat_workgroup_size: 768
    .name:           _Z7kf_mainPKfPKiPfPjS3_S4_
    .private_segment_fixed_size: 0
    .sgpr_count:     31
    .sgpr_spill_count: 0
    .symbol:         _Z7kf_mainPKfPKiPfPjS3_S4_.kd
    .uniform_work_group_size: 1
    .uses_dynamic_stack: false
    .vgpr_count:     168
    .vgpr_spill_count: 0
    .wavefront_size: 64
  - .agpr_count:     0
    .args:
      - .actual_access:  read_only
        .address_space:  global
        .offset:         0
        .size:           8
        .value_kind:     global_buffer
      - .actual_access:  read_only
        .address_space:  global
        .offset:         8
        .size:           8
        .value_kind:     global_buffer
      - .actual_access:  write_only
        .address_space:  global
        .offset:         16
        .size:           8
        .value_kind:     global_buffer
    .group_segment_fixed_size: 192
    .kernarg_segment_align: 8
    .kernarg_segment_size: 24
    .language:       OpenCL C
    .language_version:
      - 2
      - 0
    .max_flat_workgroup_size: 256
    .name:           _Z8k1_statsPKfPKiPf
    .private_segment_fixed_size: 0
    .sgpr_count:     48
    .sgpr_spill_count: 0
    .symbol:         _Z8k1_statsPKfPKiPf.kd
    .uniform_work_group_size: 1
    .uses_dynamic_stack: false
    .vgpr_count:     61
    .vgpr_spill_count: 0
    .wavefront_size: 64
  - .agpr_count:     0
    .args:
      - .actual_access:  read_only
        .address_space:  global
        .offset:         0
        .size:           8
        .value_kind:     global_buffer
      - .actual_access:  read_only
        .address_space:  global
        .offset:         8
        .size:           8
        .value_kind:     global_buffer
      - .actual_access:  read_only
        .address_space:  global
        .offset:         16
        .size:           8
        .value_kind:     global_buffer
      - .actual_access:  write_only
        .address_space:  global
        .offset:         24
        .size:           8
        .value_kind:     global_buffer
      - .actual_access:  write_only
        .address_space:  global
        .offset:         32
        .size:           8
        .value_kind:     global_buffer
    .group_segment_fixed_size: 1072
    .kernarg_segment_align: 8
    .kernarg_segment_size: 40
    .language:       OpenCL C
    .language_version:
      - 2
      - 0
    .max_flat_workgroup_size: 768
    .name:           _Z7k3_histPKfPKiS0_PjPf
    .private_segment_fixed_size: 0
    .sgpr_count:     51
    .sgpr_spill_count: 0
    .symbol:         _Z7k3_histPKfPKiS0_PjPf.kd
    .uniform_work_group_size: 1
    .uses_dynamic_stack: false
    .vgpr_count:     64
    .vgpr_spill_count: 0
    .wavefront_size: 64
  - .agpr_count:     0
    .args:
      - .actual_access:  read_only
        .address_space:  global
        .offset:         0
        .size:           8
        .value_kind:     global_buffer
      - .actual_access:  write_only
        .address_space:  global
        .offset:         8
        .size:           8
        .value_kind:     global_buffer
    .group_segment_fixed_size: 8192
    .kernarg_segment_align: 8
    .kernarg_segment_size: 16
    .language:       OpenCL C
    .language_version:
      - 2
      - 0
    .max_flat_workgroup_size: 256
    .name:           _Z9k4_reducePKjP15HIP_vector_typeIjLj2EE
    .private_segment_fixed_size: 0
    .sgpr_count:     34
    .sgpr_spill_count: 0
    .symbol:         _Z9k4_reducePKjP15HIP_vector_typeIjLj2EE.kd
    .uniform_work_group_size: 1
    .uses_dynamic_stack: false
    .vgpr_count:     52
    .vgpr_spill_count: 0
    .wavefront_size: 64
  - .agpr_count:     0
    .args:
      - .actual_access:  read_only
        .address_space:  global
        .offset:         0
        .size:           8
        .value_kind:     global_buffer
      - .actual_access:  read_only
        .address_space:  global
        .offset:         8
        .size:           8
        .value_kind:     global_buffer
      - .actual_access:  read_only
        .address_space:  global
        .offset:         16
        .size:           8
        .value_kind:     global_buffer
      - .address_space:  global
        .offset:         24
        .size:           8
        .value_kind:     global_buffer
      - .actual_access:  write_only
        .address_space:  global
        .offset:         32
        .size:           8
        .value_kind:     global_buffer
      - .offset:         40
        .size:           4
        .value_kind:     hidden_block_count_x
      - .offset:         44
        .size:           4
        .value_kind:     hidden_block_count_y
      - .offset:         48
        .size:           4
        .value_kind:     hidden_block_count_z
      - .offset:         52
        .size:           2
        .value_kind:     hidden_group_size_x
      - .offset:         54
        .size:           2
        .value_kind:     hidden_group_size_y
      - .offset:         56
        .size:           2
        .value_kind:     hidden_group_size_z
      - .offset:         58
        .size:           2
        .value_kind:     hidden_remainder_x
      - .offset:         60
        .size:           2
        .value_kind:     hidden_remainder_y
      - .offset:         62
        .size:           2
        .value_kind:     hidden_remainder_z
      - .offset:         80
        .size:           8
        .value_kind:     hidden_global_offset_x
      - .offset:         88
        .size:           8
        .value_kind:     hidden_global_offset_y
      - .offset:         96
        .size:           8
        .value_kind:     hidden_global_offset_z
      - .offset:         104
        .size:           2
        .value_kind:     hidden_grid_dims
    .group_segment_fixed_size: 12544
    .kernarg_segment_align: 8
    .kernarg_segment_size: 296
    .language:       OpenCL C
    .language_version:
      - 2
      - 0
    .max_flat_workgroup_size: 1024
    .name:           _Z8k5_finalPK15HIP_vector_typeIjLj2EEPKfS4_PyPf
    .private_segment_fixed_size: 0
    .sgpr_count:     30
    .sgpr_spill_count: 0
    .symbol:         _Z8k5_finalPK15HIP_vector_typeIjLj2EEPKfS4_PyPf.kd
    .uniform_work_group_size: 1
    .uses_dynamic_stack: false
    .vgpr_count:     44
    .vgpr_spill_count: 0
    .wavefront_size: 64
